# speedup vs baseline: 1.0246x; 1.0246x over previous
_Z6k_partPKiPKfS2_S2_S2_S2_PiS3_PDF16_S4_S4_:
	s_cmpk_gt_i32 s2, 0x7a
	s_mov_b64 s[4:5], -1
	s_cbranch_scc0 .LBB0_60
	s_cmpk_gt_u32 s2, 0x1f4
	s_cbranch_scc0 .LBB0_53
	s_load_dwordx4 s[4:7], s[0:1], 0x10
	v_lshrrev_b32_e32 v1, 4, v0
	v_and_b32_e32 v3, 15, v0
	v_lshrrev_b32_e32 v2, 1, v0
	v_and_or_b32 v1, v1, 48, v3
	v_and_b32_e32 v4, 0x78, v2
	v_lshl_add_u32 v1, v1, 6, v4
	v_lshlrev_b32_e32 v4, 2, v1
	v_mov_b32_e32 v5, 0
	v_and_b32_e32 v8, 0x60, v2
	s_waitcnt lgkmcnt(0)
	v_lshl_add_u64 v[6:7], s[4:5], 0, v[4:5]
	v_subrev_u32_e32 v4, 64, v1
	v_lshl_add_u64 v[4:5], v[4:5], 2, s[6:7]
	v_cmp_gt_u32_e32 vcc, 64, v8
	s_load_dwordx2 s[4:5], s[0:1], 0x48
	s_movk_i32 s3, 0x80
	v_cndmask_b32_e32 v13, v5, v7, vcc
	v_cndmask_b32_e32 v12, v4, v6, vcc
	global_load_dwordx4 v[4:7], v[12:13], off offset:16
	global_load_dwordx4 v[8:11], v[12:13], off
	v_lshlrev_b32_e32 v1, 4, v0
	v_cmp_gt_u32_e32 vcc, s3, v0
	s_waitcnt vmcnt(1)
	v_cvt_pk_f16_f32 v7, v6, v7
	v_cvt_pk_f16_f32 v6, v4, v5
	s_waitcnt vmcnt(0)
	v_cvt_pk_f16_f32 v5, v10, v11
	v_cvt_pk_f16_f32 v4, v8, v9
	s_waitcnt lgkmcnt(0)
	global_store_dwordx4 v1, v[4:7], s[4:5] sc1
	s_and_saveexec_b64 s[6:7], vcc
	s_cbranch_execz .LBB0_52
	s_load_dwordx4 s[8:11], s[0:1], 0x20
	v_lshrrev_b32_e32 v4, 2, v0
	v_and_b32_e32 v4, 12, v4
	v_and_or_b32 v2, v2, 32, v4
	v_cmp_lt_u32_e64 s[4:5], 1, v3
	v_cmp_gt_u32_e32 vcc, 4, v3
	v_lshlrev_b32_e32 v8, 6, v3
	s_and_saveexec_b64 s[12:13], s[4:5]
	s_xor_b64 s[12:13], exec, s[12:13]
	s_cbranch_execz .LBB0_7
	v_mov_b32_e32 v6, 0
	s_and_saveexec_b64 s[14:15], vcc
	s_cbranch_execz .LBB0_6
	v_add_lshl_u32 v3, v2, v8, 2
	s_waitcnt lgkmcnt(0)
	global_load_dword v6, v3, s[10:11] offset:-512

.LBB0_53:
	s_andn2_b64 vcc, exec, s[4:5]
	s_cbranch_vccnz .LBB0_59
	s_load_dwordx2 s[6:7], s[0:1], 0x8
	s_load_dwordx2 s[4:5], s[0:1], 0x40
	s_sub_i32 s3, s2, 0x7b
	s_lshl_b32 s3, s3, 10
	v_or_b32_e32 v30, s3, v0
	v_lshlrev_b32_e32 v31, 4, v30
	v_lshlrev_b32_e32 v32, 3, v30
	v_add_u32_e32 v33, 0x5e8000, v31
	v_add_u32_e32 v34, 0xbd0000, v31
	v_add_u32_e32 v35, 0x11b8000, v31
	v_add_u32_e32 v36, 0x17a0000, v31
	s_mov_b32 s8, 0xca00
	v_cmp_gt_u32_e32 vcc, s8, v30
	s_waitcnt lgkmcnt(0)
	global_load_dwordx4 v[2:5], v31, s[6:7] nt
	global_load_dwordx4 v[6:9], v33, s[6:7] nt
	global_load_dwordx4 v[10:13], v34, s[6:7] nt
	global_load_dwordx4 v[14:17], v35, s[6:7] nt
	s_and_saveexec_b64 s[8:9], vcc
	s_cbranch_execz .Lk1c_a
	global_load_dwordx4 v[18:21], v36, s[6:7] nt
.Lk1c_a:
	s_mov_b64 exec, s[8:9]
	v_add_u32_e32 v33, 0x2f4000, v32
	v_add_u32_e32 v34, 0x5e8000, v32
	v_add_u32_e32 v35, 0x8dc000, v32
	v_add_u32_e32 v36, 0xbd0000, v32
	s_waitcnt vmcnt(0)
	v_cvt_pk_f16_f32 v2, v2, v3
	v_cvt_pk_f16_f32 v3, v4, v5
	global_store_dwordx2 v32, v[2:3], s[4:5] sc1
	v_cvt_pk_f16_f32 v6, v6, v7
	v_cvt_pk_f16_f32 v7, v8, v9
	global_store_dwordx2 v33, v[6:7], s[4:5] sc1
	v_cvt_pk_f16_f32 v10, v10, v11
	v_cvt_pk_f16_f32 v11, v12, v13
	global_store_dwordx2 v34, v[10:11], s[4:5] sc1
	v_cvt_pk_f16_f32 v14, v14, v15
	v_cvt_pk_f16_f32 v15, v16, v17
	global_store_dwordx2 v35, v[14:15], s[4:5] sc1
	s_and_saveexec_b64 s[8:9], vcc
	s_cbranch_execz .Lk1c_b
	v_cvt_pk_f16_f32 v18, v18, v19
	v_cvt_pk_f16_f32 v19, v20, v21
	global_store_dwordx2 v36, v[18:19], s[4:5] sc1
